# barrier elision in P2 (attention unit prologue barrier and conversion chunk-end barrier are implied by the queue pop's two barriers) + next queue pop issued when the tile loop ends
# baseline (speedup 1.0000x reference)
; __device__ void conv_jobs_deep(const Params& p, unsigned char* smem, int j0, int j1) {
;     ...
;     }
;     __syncthreads();
; __device__ void phase2(const Params& p, unsigned char* smem, unsigned* qw) {
;     ...
;     for (;;) {
;         const bool take_conv = conv_left && (conv_first || !att_left);
;         if (!take_conv && !att_left) break;
;         const int q = (x + aq) & 7;
;         __syncthreads();
.LBB0_370:
	s_mov_b64 s[54:55], -1
	s_nop 0

; template <bool ISA>
; __device__ __forceinline__ void attn_unit(const Params& p, unsigned char* smem, int b, int hh, int blk) {
;     ...
;     if (ISA) { const int g = hh >> 2; kbase = p.ka + (size_t)(b * TT) * 128 + g * 64; ldk = 128; vbase = p.vta + (size_t)((b * 2 + g) * 64) * TT; }
;     else { kbase = p.kb + (size_t)(b * TT) * 512 + hh * 64; ldk = 512; vbase = p.vtb + (size_t)((b * 8 + hh) * 64) * TT; }
;     float* rpbl = (float*)(smem + 49152);
;     const float M2 = p.attm[ISA ? hh : 8 + hh], negM2 = -M2;
;     const int qt0 = ISA ? blk * 128 + wid * 32 : blk * 128 + wid * 16;
;     bf16x8 qf[NQ][2];
;     {
;         const bf16_t* qsrc = ISA ? p.qa : p.qb;
; #pragma unroll
;         for (int q = 0; q < NQ; ++q)
; #pragma unroll
;             for (int ks = 0; ks < 2; ++ks)
;                 qf[q][ks] = *(const bf16x8*)(qsrc + (size_t)(b * TT + qt0 + q * QSTR + l15) * 512 + hh * 64 + ks * 32 + gq * 8);
;     }
;     f32x4 osum[NQ]; f32x4 o[NQ][4];
; #pragma unroll
;     for (int q = 0; q < NQ; ++q) {
;         const float l0 = ISA ? __builtin_amdgcn_exp2f(p.sink[hh] * L2E - M2) : 0.f;
;         osum[q] = (f32x4){l0, l0, l0, l0};
; #pragma unroll
;         for (int df = 0; df < 4; ++df) o[q][df] = (f32x4){0.f, 0.f, 0.f, 0.f};
;     }
;     const int qcol = wid * 16 + l15;
;     int cs = wid * 16 - 8; cs = cs < 0 ? 0 : (cs > 32 ? 32 : cs);
;     int wstart = qcol - 8; wstart = wstart < 0 ? 0 : (wstart > 48 ? 48 : wstart);
;     NaConst nc;
; #pragma unroll
;     for (int j = 0; j < 4; ++j) {
;         const int kc = cs + (j >> 1) * 16 + gq * 4 + (j & 1) * 2;
;         nc.cm[j] = (((kc >= wstart) && (kc < wstart + 16)) ? 0xFFFFu : 0u) | (((kc + 1 >= wstart) && (kc + 1 < wstart + 16)) ? 0xFFFF0000u : 0u);
;     }
;     nc.blane = (unsigned)(size_t)(LAS unsigned char*)smem + 49152u + (unsigned)((16 + (cs + gq * 4 - qcol + 15)) * 4);
;     LAS unsigned char* ldsu = (LAS unsigned char*)smem;
;     const unsigned ldsa = (unsigned)(size_t)ldsu;
;     const int wuni = __builtin_amdgcn_readfirstlane(wid);
;     const bf16_t* kp0; const bf16_t* kp1; const bf16_t* vp0; const bf16_t* vp1;
;     {
;         const int ra = (wid * 2) * 8 + (lane >> 3), rb = (wid * 2 + 1) * 8 + (lane >> 3);
;         const int ca = ((lane & 7) ^ ((ra >> 1) & 7)) * 8, cb = ((lane & 7) ^ ((rb >> 1) & 7)) * 8;
;         kp0 = kbase + (size_t)ra * ldk + ca; kp1 = kbase + (size_t)rb * ldk + cb;
.LBB0_377:
	s_or_b64 exec, exec, s[6:7]
	s_mov_b32 s98, 0
	s_waitcnt lgkmcnt(0)
	s_barrier
	ds_read_b32 v2, v118
	s_xor_b64 s[6:7], s[0:1], -1
	s_mov_b64 s[0:1], -1
	s_and_b64 vcc, exec, s[6:7]
	s_waitcnt lgkmcnt(0)
	v_readfirstlane_b32 s4, v2
	s_cbranch_vccz .LBB0_429
	s_cmpk_lt_i32 s4, 0x100
	s_cbranch_scc0 .LBB0_426
	s_cmpk_gt_i32 s4, 0x7f
	s_cbranch_scc0 .LBB0_401
	s_add_i32 s0, s4, 0xffffff80
	s_lshr_b32 s24, s0, 5
	s_lshl_b32 s76, s5, 6
	s_lshl_b32 s6, s24, 9
	s_lshl_b32 s0, s4, 1
	s_or_b32 s6, s6, s76
	s_and_b32 s0, s0, 62
	s_mulk_i32 s6, 0x2100
	s_mov_b32 s7, s77
	v_add_u32_e32 v21, s0, v1
	v_mov_b32_e32 v30, v0
	s_lshl_b64 s[6:7], s[6:7], 1
	v_readlane_b32 s9, v248, 26
	v_lshlrev_b32_e32 v101, 1, v21
	v_bfe_u32 v31, v30, 6, 2
	s_add_u32 s6, s9, s6
	v_readlane_b32 s9, v248, 28
	v_add_u32_e32 v19, -4, v101
	s_addc_u32 s7, s9, s7
	s_or_b32 s23, s5, 8
	v_lshlrev_b32_e32 v20, 4, v31
	v_min_i32_e32 v2, 0x77, v19
	s_mul_i32 s8, s24, 0x2100
	s_lshl_b32 s9, s23, 2
	v_lshl_or_b32 v100, v21, 7, v20
	v_lshlrev_b32_e32 v22, 6, v2
	v_mov_b32_e32 v4, s9
	v_add_u32_e32 v2, s8, v100
	s_lshl_b32 s10, s5, 7
	v_readlane_b32 s8, v248, 9
	v_and_b32_e32 v112, 15, v30
	v_readlane_b32 s9, v248, 10
	s_add_u32 s8, s8, s10
	v_or_b32_e32 v6, v2, v112
	s_addc_u32 s9, s9, 0
	v_and_b32_e32 v98, 48, v30
	v_lshl_add_u64 v[8:9], s[8:9], 0, v[98:99]
	v_ashrrev_i32_e32 v7, 31, v6
	v_readlane_b32 s8, v248, 20
	s_mul_i32 s0, s24, 0x420000
	s_mov_b32 s1, s77
	v_lshlrev_b64 v[2:3], 10, v[6:7]
	v_readlane_b32 s9, v248, 21
	v_lshl_add_u64 v[10:11], v[8:9], 0, v[2:3]
	s_nop 3
	global_load_dword v113, v4, s[8:9]
	s_nop 0
	global_load_dwordx4 v[2:5], v[10:11], off
	s_lshl_b64 s[0:1], s[0:1], 1
	v_readlane_b32 s8, v248, 7
	v_readlane_b32 s9, v248, 8
	s_add_u32 s0, s8, s0
	v_cmp_gt_i32_e32 vcc, 2, v21
	v_bfe_u32 v21, v30, 3, 3
	s_addc_u32 s1, s9, s1
	v_or_b32_e32 v21, v20, v21
	v_bfe_u32 v18, v30, 4, 2
	s_add_u32 s0, s0, s10
	v_or_b32_e32 v28, 8, v21
	s_addc_u32 s1, s1, 0
	v_cndmask_b32_e64 v102, v22, 0, vcc
	v_bitop3_b32 v24, v18, v30, 7 bitop3:0x78
	v_lshrrev_b32_e32 v22, 1, v28
	v_lshlrev_b32_e32 v98, 10, v21
	v_xor_b32_e32 v25, v22, v30
	v_lshl_add_u64 v[22:23], s[0:1], 0, v[98:99]
	v_lshlrev_b32_e32 v98, 4, v24
	v_lshl_add_u64 v[104:105], v[22:23], 0, v[98:99]
	v_lshlrev_b32_e32 v22, 10, v28
	v_mov_b32_e32 v23, v99
	v_lshlrev_b32_e32 v24, 4, v25
	v_or_b32_e32 v6, 64, v6
	v_readfirstlane_b32 s8, v31
	v_lshl_add_u64 v[22:23], s[0:1], 0, v[22:23]
	v_and_b32_e32 v24, 0x70, v24
	v_mov_b32_e32 v25, v99
	v_ashrrev_i32_e32 v7, 31, v6
	v_lshl_add_u64 v[106:107], v[22:23], 0, v[24:25]
	v_mov_b64_e32 v[22:23], s[6:7]
	s_movk_i32 s6, 0x4200
	s_lshl_b32 s25, s8, 11
	v_lshlrev_b64 v[6:7], 10, v[6:7]
	v_mad_u64_u32 v[26:27], s[0:1], v21, s6, v[22:23]
	v_mad_u64_u32 v[22:23], s[0:1], v28, s6, v[22:23]
	v_ashrrev_i32_e32 v103, 31, v102
	v_add_u32_e32 v21, s25, v114
	v_lshl_add_u64 v[14:15], v[8:9], 0, v[6:7]
	v_lshl_add_u64 v[108:109], v[26:27], 0, v[98:99]
	v_lshl_add_u64 v[110:111], v[22:23], 0, v[24:25]
	v_lshlrev_b64 v[22:23], 10, v[102:103]
	v_readfirstlane_b32 s0, v21
	v_add_u32_e32 v26, 0x400, v21
	global_load_dwordx4 v[6:9], v[10:11], off offset:64
	s_nop 0
	global_load_dwordx4 v[10:13], v[14:15], off
	s_nop 0
	global_load_dwordx4 v[14:17], v[14:15], off offset:64
	s_waitcnt lgkmcnt(0)
	s_nop 0
	v_lshl_add_u64 v[24:25], v[104:105], 0, v[22:23]
	s_mov_b32 m0, s0
	v_readfirstlane_b32 s0, v26
	global_load_lds_dwordx4 v[24:25], off
	v_lshl_add_u64 v[24:25], v[106:107], 0, v[22:23]
	s_mov_b32 m0, s0
	v_add_u32_e32 v28, 0x6000, v21
	global_load_lds_dwordx4 v[24:25], off
	v_lshlrev_b64 v[24:25], 1, v[102:103]
	v_readfirstlane_b32 s0, v28
	v_add_u32_e32 v28, 0x6400, v21
	v_lshl_add_u64 v[26:27], v[108:109], 0, v[24:25]
	s_mov_b32 m0, s0
	v_readfirstlane_b32 s0, v28
	global_load_lds_dwordx4 v[26:27], off
	s_mov_b32 m0, s0
	s_mov_b64 s[0:1], 0x10000
	v_add_u32_e32 v32, 0x2000, v21
	v_lshl_add_u64 v[24:25], v[110:111], 0, v[24:25]
	v_lshl_add_u64 v[22:23], v[22:23], 0, s[0:1]
	v_readfirstlane_b32 s0, v32
	global_load_lds_dwordx4 v[24:25], off
	v_lshl_add_u64 v[28:29], v[104:105], 0, v[22:23]
	s_mov_b32 m0, s0
	v_lshl_add_u64 v[22:23], v[106:107], 0, v[22:23]
	global_load_lds_dwordx4 v[28:29], off
	v_add_u32_e32 v28, 0x2400, v21
	s_mov_b64 s[6:7], 0x80
	v_readfirstlane_b32 s0, v28
	s_mov_b32 m0, s0
	v_and_b32_e32 v103, 63, v30
	global_load_lds_dwordx4 v[22:23], off
	v_lshl_add_u64 v[22:23], v[26:27], 0, s[6:7]
	v_add_u32_e32 v26, 0x8000, v21
	v_add_u32_e32 v21, 0x8400, v21
	v_readfirstlane_b32 s0, v26
	s_mov_b32 m0, s0
	v_readfirstlane_b32 s0, v21
	global_load_lds_dwordx4 v[22:23], off
	v_lshl_add_u64 v[22:23], v[24:25], 0, s[6:7]
	s_mov_b32 m0, s0
	s_mul_i32 s6, s5, 0x1d1
	global_load_lds_dwordx4 v[22:23], off
	v_and_b32_e32 v23, 0xff, v30
	v_add_u32_e32 v22, -16, v103
	s_add_i32 s6, s6, -16
	v_mul_u32_u24_e32 v24, 31, v31
	v_lshlrev_b32_e32 v21, 3, v18
	v_cmp_gt_u32_e64 s[0:1], 31, v22
	v_lshl_add_u32 v22, v23, 2, v117
	v_add3_u32 v98, s6, v24, v103
	v_or_b32_e32 v23, 0xffffff00, v23
	v_mov_b32_e32 v26, 0
	v_mov_b32_e32 v27, 0
	v_mov_b32_e32 v28, 0
	v_mov_b32_e32 v29, 0
	v_and_b32_e32 v32, 0xff, v30
	s_movk_i32 s8, 0xc0
	v_lshl_add_u64 v[24:25], v[98:99], 2, s[80:81]
	v_cmp_gt_u32_e64 s[8:9], s8, v32
	s_and_saveexec_b64 s[6:7], s[0:1]
	global_load_dword v26, v[24:25], off
	global_load_dword v27, v[24:25], off offset:496
	global_load_dword v28, v[24:25], off offset:992
	s_and_b64 exec, exec, s[8:9]
	global_load_dword v29, v[24:25], off offset:1488
	s_mov_b64 exec, s[6:7]
	s_waitcnt vmcnt(0)
; #define LAS __attribute__((address_space(3)))
; template <bool ISA>
; __device__ __forceinline__ void attn_unit(const Params& p, unsigned char* smem, int b, int hh, int blk) {
;     ...
;     const int qcol = wid * 16 + l15;
;     int cs = wid * 16 - 8; cs = cs < 0 ? 0 : (cs > 32 ? 32 : cs);
;     int wstart = qcol - 8; wstart = wstart < 0 ? 0 : (wstart > 48 ? 48 : wstart);
;     NaConst nc;
; #pragma unroll
;     for (int j = 0; j < 4; ++j) {
;         const int kc = cs + (j >> 1) * 16 + gq * 4 + (j & 1) * 2;
;         nc.cm[j] = (((kc >= wstart) && (kc < wstart + 16)) ? 0xFFFFu : 0u) | (((kc + 1 >= wstart) && (kc + 1 < wstart + 16)) ? 0xFFFF0000u : 0u);
;     }
;     nc.blane = (unsigned)(size_t)(LAS unsigned char*)smem + 49152u + (unsigned)((16 + (cs + gq * 4 - qcol + 15)) * 4);
;     LAS unsigned char* ldsu = (LAS unsigned char*)smem;
;     const unsigned ldsa = (unsigned)(size_t)ldsu;
;     const int wuni = __builtin_amdgcn_readfirstlane(wid);
;     const bf16_t* kp0; const bf16_t* kp1; const bf16_t* vp0; const bf16_t* vp1;
;     {
;         const int ra = (wid * 2) * 8 + (lane >> 3), rb = (wid * 2 + 1) * 8 + (lane >> 3);
;         const int ca = ((lane & 7) ^ ((ra >> 1) & 7)) * 8, cb = ((lane & 7) ^ ((rb >> 1) & 7)) * 8;
;         kp0 = kbase + (size_t)ra * ldk + ca; kp1 = kbase + (size_t)rb * ldk + cb;
;         vp0 = vbase + (size_t)ra * TT + ca; vp1 = vbase + (size_t)rb * TT + cb;
;     }
;     ...
;     asm volatile("s_waitcnt lgkmcnt(0)" ::: "memory"); __builtin_amdgcn_s_barrier(); asm volatile("" ::: "memory");
;     ADMA(0);
;     if (ntile > 1) ADMA(1);
;     if (!ISA) {
;         for (int i = tid; i < 15 * 64; i += 256) { const int dr = i >> 6, dc = (i & 63) - 16; rpbl[i] = ((dc >= 0 && dc < 31) ? p.rpb[hh * 465 + dr * 31 + dc] * L2E : 0.f) - M2; }
	v_mul_f32_e32 v26, 0x3fb8aa3b, v26
	v_mul_f32_e32 v27, 0x3fb8aa3b, v27
	v_mul_f32_e32 v28, 0x3fb8aa3b, v28
	v_mul_f32_e32 v29, 0x3fb8aa3b, v29
	v_sub_f32_e32 v26, v26, v113
	v_sub_f32_e32 v27, v27, v113
	v_sub_f32_e32 v28, v28, v113
	v_sub_f32_e32 v29, v29, v113
	ds_write_b32 v22, v26
	ds_write_b32 v22, v27 offset:1024
	ds_write_b32 v22, v28 offset:2048
	s_and_saveexec_b64 s[6:7], s[8:9]
	ds_write_b32 v22, v29 offset:3072
	s_or_b64 exec, exec, s[6:7]
	v_or_b32_e32 v22, v20, v112
	v_med3_u32 v20, v20, 8, 40
	v_add_u32_e32 v20, -8, v20
	v_med3_u32 v23, v22, 8, 56
	v_lshlrev_b32_e32 v98, 2, v18
	v_add_u32_e32 v24, v20, v98
	v_add_u32_e32 v25, 8, v23
	v_add_u32_e32 v23, -8, v23
	v_cmp_lt_u32_e64 s[0:1], v24, v25
	v_or_b32_e32 v26, 1, v24
	v_cmp_ge_u32_e64 s[20:21], v24, v23
	v_cmp_lt_u32_e64 s[6:7], v26, v25
	v_add_u32_e32 v29, 16, v24
	s_and_b64 s[0:1], s[20:21], s[0:1]
	v_cmp_ge_u32_e64 s[20:21], v26, v23
	v_or_b32_e32 v27, 2, v24
	v_or_b32_e32 v28, 3, v24
	v_add_u32_e32 v30, 17, v24
	v_or_b32_e32 v31, 2, v29
	v_add_u32_e32 v32, 19, v24
	s_and_b64 s[6:7], s[20:21], s[6:7]
	v_cmp_lt_u32_e64 s[8:9], v27, v25
	v_cmp_lt_u32_e64 s[10:11], v28, v25
	v_cmp_lt_u32_e64 s[12:13], v29, v25
	v_cmp_lt_u32_e64 s[14:15], v30, v25
	v_cmp_lt_u32_e64 s[16:17], v31, v25
	v_cmp_lt_u32_e64 s[18:19], v32, v25
	v_cndmask_b32_e64 v25, 0, v119, s[6:7]
	v_cmp_ge_u32_e64 s[6:7], v27, v23
	s_and_b64 s[6:7], s[6:7], s[8:9]
	v_cmp_ge_u32_e64 s[8:9], v28, v23
	s_and_b64 s[8:9], s[8:9], s[10:11]
	v_cmp_ge_u32_e64 s[10:11], v30, v23
	v_cndmask_b32_e64 v26, 0, v119, s[8:9]
	v_cmp_ge_u32_e64 s[8:9], v29, v23
	s_and_b64 s[10:11], s[10:11], s[14:15]
	v_cndmask_b32_e64 v28, 0, v120, s[0:1]
	s_and_b64 s[8:9], s[8:9], s[12:13]
	v_cndmask_b32_e64 v27, 0, v119, s[10:11]
	v_cmp_ge_u32_e64 s[10:11], v31, v23
	v_cmp_ge_u32_e64 s[12:13], v32, v23
	v_or_b32_e32 v125, v25, v28
	v_cndmask_b32_e64 v25, 0, v120, s[6:7]
	v_sub_u32_e32 v22, v24, v22
	s_and_b64 s[10:11], s[10:11], s[16:17]
	s_and_b64 s[12:13], s[12:13], s[18:19]
	v_or_b32_e32 v126, v26, v25
	v_cndmask_b32_e64 v25, 0, v120, s[8:9]
	v_min_i32_e32 v19, 0x78, v19
	v_cndmask_b32_e64 v23, 0, v119, s[12:13]
	v_or_b32_e32 v127, v27, v25
	v_cndmask_b32_e64 v25, 0, v120, s[10:11]
	v_lshl_add_u32 v129, v22, 2, v115
	v_lshrrev_b32_e32 v22, 1, v112
	v_cndmask_b32_e64 v137, v19, 0, vcc
	v_med3_i32 v19, v101, 3, v121
	v_or_b32_e32 v128, v25, v23
	v_xor_b32_e32 v25, v18, v22
	v_add_u32_e32 v138, -3, v19
	v_add_u32_e32 v140, 5, v19
	v_add_u16_e32 v19, v20, v112
	v_lshlrev_b32_e32 v131, 4, v25
	v_bitop3_b32 v25, v18, v22, 4 bitop3:0x36
	v_lshrrev_b16_e32 v19, 1, v19
	v_or_b32_e32 v23, 4, v18
	v_lshlrev_b32_e32 v132, 4, v25
	v_lshrrev_b32_e32 v25, 5, v103
	v_bitop3_b32 v18, v19, v18, 7 bitop3:0x6c
	v_xor_b32_e32 v26, v25, v22
	v_lshlrev_b32_e32 v142, 4, v18
	v_bitop3_b32 v18, v19, v23, 7 bitop3:0x6c
	v_lshlrev_b32_e32 v130, 7, v112
	v_and_b32_e32 v21, 8, v21
	v_lshlrev_b32_e32 v26, 4, v26
	v_lshlrev_b32_e32 v143, 4, v18
	v_lshrrev_b32_e32 v18, 3, v24
	v_or3_b32 v134, v26, v130, v21
	v_bitop3_b32 v26, v25, v22, 2 bitop3:0x36
	v_xor_b32_e32 v18, v18, v22
	v_lshlrev_b32_e32 v135, 4, v26
	v_bitop3_b32 v26, v25, v22, 4 bitop3:0x36
	v_lshlrev_b32_e32 v144, 4, v18
	v_lshlrev_b32_e32 v18, 1, v24
	v_lshlrev_b32_e32 v26, 4, v26
	v_and_or_b32 v145, v18, 8, v130
	v_lshrrev_b32_e32 v18, 3, v29
	v_or_b32_e32 v133, v21, v130
	v_bitop3_b32 v25, v25, v22, 6 bitop3:0x36
	v_add_lshl_u32 v141, v20, v112, 7
	v_xor_b32_e32 v18, v18, v22
	v_or3_b32 v147, v130, v26, v21
	v_mov_b32_e32 v20, v99
	v_mov_b32_e32 v21, v99
	v_lshlrev_b32_e32 v136, 4, v25
	v_lshlrev_b32_e32 v146, 4, v18
	v_mov_b32_e32 v18, v99
	v_mov_b32_e32 v19, v99
	v_mov_b32_e32 v50, 0
	v_mov_b64_e32 v[24:25], v[20:21]
	v_mov_b64_e32 v[28:29], v[20:21]
	v_mov_b64_e32 v[32:33], v[20:21]
	v_mov_b64_e32 v[36:37], v[20:21]
	v_mov_b64_e32 v[40:41], v[20:21]
	v_mov_b64_e32 v[44:45], v[20:21]
	v_mov_b64_e32 v[48:49], v[20:21]
	s_mov_b32 s26, 2
	v_add_u32_e32 v139, 8, v137
	s_movk_i32 s8, 0x1e40
	v_mov_b64_e32 v[22:23], v[18:19]
	v_mov_b64_e32 v[26:27], v[18:19]
	v_mov_b64_e32 v[30:31], v[18:19]
	v_mov_b64_e32 v[34:35], v[18:19]
	v_mov_b64_e32 v[38:39], v[18:19]
	v_mov_b64_e32 v[42:43], v[18:19]
	v_mov_b64_e32 v[46:47], v[18:19]
	v_mov_b32_e32 v51, v50
	v_mov_b32_e32 v52, v50
	v_mov_b32_e32 v53, v50
	v_mov_b32_e32 v54, v50
	v_mov_b32_e32 v55, v50
	v_mov_b32_e32 v56, v50
	v_mov_b32_e32 v57, v50
	s_cmpk_eq_i32 s8, 0x2140
	s_mov_b64 s[0:1], -1
	s_cbranch_scc1 .LBB0_386

; template <bool ISA>
; __device__ __forceinline__ void attn_unit(const Params& p, unsigned char* smem, int b, int hh, int blk) {
;     ...
;     if (ISA) { const int g = hh >> 2; kbase = p.ka + (size_t)(b * TT) * 128 + g * 64; ldk = 128; vbase = p.vta + (size_t)((b * 2 + g) * 64) * TT; }
;     else { kbase = p.kb + (size_t)(b * TT) * 512 + hh * 64; ldk = 512; vbase = p.vtb + (size_t)((b * 8 + hh) * 64) * TT; }
;     float* rpbl = (float*)(smem + 49152);
;     const float M2 = p.attm[ISA ? hh : 8 + hh], negM2 = -M2;
;     const int qt0 = ISA ? blk * 128 + wid * 32 : blk * 128 + wid * 16;
;     bf16x8 qf[NQ][2];
;     {
;         const bf16_t* qsrc = ISA ? p.qa : p.qb;
; #pragma unroll
;         for (int q = 0; q < NQ; ++q)
; #pragma unroll
;             for (int ks = 0; ks < 2; ++ks)
;                 qf[q][ks] = *(const bf16x8*)(qsrc + (size_t)(b * TT + qt0 + q * QSTR + l15) * 512 + hh * 64 + ks * 32 + gq * 8);
;     }
;     f32x4 osum[NQ]; f32x4 o[NQ][4];
; #pragma unroll
;     for (int q = 0; q < NQ; ++q) {
;         const float l0 = ISA ? __builtin_amdgcn_exp2f(p.sink[hh] * L2E - M2) : 0.f;
;         osum[q] = (f32x4){l0, l0, l0, l0};
; #pragma unroll
;         for (int df = 0; df < 4; ++df) o[q][df] = (f32x4){0.f, 0.f, 0.f, 0.f};
;     }
;     const int qcol = wid * 16 + l15;
;     int cs = wid * 16 - 8; cs = cs < 0 ? 0 : (cs > 32 ? 32 : cs);
;     int wstart = qcol - 8; wstart = wstart < 0 ? 0 : (wstart > 48 ? 48 : wstart);
;     NaConst nc;
; #pragma unroll
;     for (int j = 0; j < 4; ++j) {
;         const int kc = cs + (j >> 1) * 16 + gq * 4 + (j & 1) * 2;
;         nc.cm[j] = (((kc >= wstart) && (kc < wstart + 16)) ? 0xFFFFu : 0u) | (((kc + 1 >= wstart) && (kc + 1 < wstart + 16)) ? 0xFFFF0000u : 0u);
;     }
;     nc.blane = (unsigned)(size_t)(LAS unsigned char*)smem + 49152u + (unsigned)((16 + (cs + gq * 4 - qcol + 15)) * 4);
;     LAS unsigned char* ldsu = (LAS unsigned char*)smem;
;     const unsigned ldsa = (unsigned)(size_t)ldsu;
;     const int wuni = __builtin_amdgcn_readfirstlane(wid);
;     const bf16_t* kp0; const bf16_t* kp1; const bf16_t* vp0; const bf16_t* vp1;
;     {
;         const int ra = (wid * 2) * 8 + (lane >> 3), rb = (wid * 2 + 1) * 8 + (lane >> 3);
;         const int ca = ((lane & 7) ^ ((ra >> 1) & 7)) * 8, cb = ((lane & 7) ^ ((rb >> 1) & 7)) * 8;
;         kp0 = kbase + (size_t)ra * ldk + ca; kp1 = kbase + (size_t)rb * ldk + cb;
.LBB0_401:
	s_and_b64 vcc, exec, s[0:1]
	s_cbranch_vccz .LBB0_425
	v_lshl_add_u32 v2, s4, 1, v1
	v_mov_b32_e32 v31, v0
	v_ashrrev_i32_e32 v30, 2, v2
	s_lshr_b32 s5, s5, 1
	v_bfe_u32 v19, v31, 6, 2
	s_lshl_b32 s0, s22, 2
	v_lshlrev_b32_e32 v18, 7, v30
	v_lshlrev_b32_e32 v33, 5, v19
	s_and_b32 s6, s0, 4
	s_mul_i32 s0, s5, 0x2100
	v_or_b32_e32 v84, v33, v18
	v_and_or_b32 v82, v2, 3, s6
	v_and_b32_e32 v83, 15, v31
	v_add_u32_e32 v2, s0, v84
	v_readlane_b32 s8, v248, 11
	s_lshl_b32 s1, s6, 4
	s_lshl_b32 s7, s5, 7
	v_or_b32_e32 v2, v2, v83
	v_lshlrev_b32_e32 v4, 7, v82
	v_mov_b32_e32 v5, v99
	v_readlane_b32 s9, v248, 12
	s_or_b32 s1, s1, s7
	v_and_b32_e32 v6, 48, v31
	v_lshl_add_u64 v[4:5], s[8:9], 0, v[4:5]
	v_mov_b32_e32 v7, v99
	v_ashrrev_i32_e32 v3, 31, v2
	s_mul_i32 s0, s5, 0x210000
	v_readlane_b32 s8, v248, 5
	v_lshl_add_u64 v[4:5], v[4:5], 0, v[6:7]
	v_lshlrev_b64 v[6:7], 10, v[2:3]
	v_or_b32_e32 v2, 16, v2
	v_readlane_b32 s9, v248, 6
	s_add_u32 s7, s8, s0
	v_ashrrev_i32_e32 v3, 31, v2
	s_addc_u32 s8, s9, 0
	s_mulk_i32 s1, 0x4200
	v_readlane_b32 s0, v248, 24
	v_lshlrev_b64 v[2:3], 10, v[2:3]
	s_add_u32 s0, s0, s1
	v_readlane_b32 s1, v248, 0
	v_readlane_b32 s10, v248, 20
	v_lshlrev_b32_e32 v21, 2, v82
	v_lshl_add_u64 v[14:15], v[4:5], 0, v[6:7]
	v_lshl_add_u64 v[10:11], v[4:5], 0, v[2:3]
	s_addc_u32 s1, s1, 0
	v_readlane_b32 s11, v248, 21
	s_lshl_b32 s6, s6, 5
	global_load_dwordx4 v[2:5], v[14:15], off offset:64
	global_load_dwordx4 v[6:9], v[10:11], off
	s_nop 0
	global_load_dwordx4 v[10:13], v[10:11], off offset:64
	s_nop 0
	global_load_dword v100, v21, s[10:11]
	s_nop 0
	global_load_dwordx4 v[14:17], v[14:15], off
	s_nop 0
	global_load_dword v34, v21, s[78:79]
	s_add_u32 s6, s7, s6
	v_bfe_u32 v21, v31, 3, 3
	s_addc_u32 s7, s8, 0
	v_readfirstlane_b32 s8, v19
	v_lshl_or_b32 v19, v19, 4, v21
	v_or_b32_e32 v21, 8, v19
	v_bfe_u32 v32, v31, 4, 2
	v_lshrrev_b32_e32 v22, 1, v21
	v_bitop3_b32 v24, v32, v31, 7 bitop3:0x78
	v_xor_b32_e32 v26, v22, v31
	v_lshlrev_b32_e32 v22, 8, v19
	s_waitcnt lgkmcnt(0)
	v_mov_b32_e32 v23, v99
	v_lshl_add_u64 v[22:23], s[6:7], 0, v[22:23]
	v_lshlrev_b32_e32 v24, 4, v24
	v_mov_b32_e32 v25, v99
	v_lshl_add_u64 v[90:91], v[22:23], 0, v[24:25]
	v_lshlrev_b32_e32 v22, 8, v21
	v_mov_b32_e32 v23, v99
	v_lshlrev_b32_e32 v26, 4, v26
	v_cmp_lt_i32_e32 vcc, 0, v30
	v_lshl_add_u64 v[22:23], s[6:7], 0, v[22:23]
	v_and_b32_e32 v26, 0x70, v26
	v_mov_b32_e32 v27, v99
	v_cndmask_b32_e64 v85, 2, 0, vcc
	v_lshl_add_u64 v[92:93], v[22:23], 0, v[26:27]
	v_mov_b64_e32 v[22:23], s[0:1]
	s_movk_i32 s6, 0x4200
	v_add_u32_e32 v89, 0xffffff80, v18
	v_lshlrev_b32_e32 v20, 6, v85
	v_mad_u64_u32 v[28:29], s[0:1], v19, s6, v[22:23]
	v_mad_u64_u32 v[22:23], s[0:1], v21, s6, v[22:23]
	s_lshl_b32 s76, s8, 11
	v_add_u32_e32 v86, v20, v89
	v_lshl_add_u64 v[96:97], v[22:23], 0, v[26:27]
	v_add_u32_e32 v26, s76, v114
	v_ashrrev_i32_e32 v87, 31, v86
	v_readfirstlane_b32 s0, v26
	v_add_u32_e32 v19, 0x400, v26
	v_lshlrev_b64 v[22:23], 8, v[86:87]
	s_mov_b32 m0, s0
	v_readfirstlane_b32 s0, v19
	v_mov_b32_e32 v21, v99
	v_ashrrev_i32_e32 v19, 31, v18
	v_lshl_add_u64 v[94:95], v[28:29], 0, v[24:25]
	s_waitcnt lgkmcnt(0)
; #define LAS __attribute__((address_space(3)))
; template <bool ISA>
; __device__ __forceinline__ void attn_unit(const Params& p, unsigned char* smem, int b, int hh, int blk) {
;     ...
;     f32x4 osum[NQ]; f32x4 o[NQ][4];
; #pragma unroll
;     for (int q = 0; q < NQ; ++q) {
;         const float l0 = ISA ? __builtin_amdgcn_exp2f(p.sink[hh] * L2E - M2) : 0.f;
;         osum[q] = (f32x4){l0, l0, l0, l0};
; #pragma unroll
;         for (int df = 0; df < 4; ++df) o[q][df] = (f32x4){0.f, 0.f, 0.f, 0.f};
;     }
;     const int qcol = wid * 16 + l15;
;     int cs = wid * 16 - 8; cs = cs < 0 ? 0 : (cs > 32 ? 32 : cs);
;     int wstart = qcol - 8; wstart = wstart < 0 ? 0 : (wstart > 48 ? 48 : wstart);
;     NaConst nc;
; #pragma unroll
;     for (int j = 0; j < 4; ++j) {
;         const int kc = cs + (j >> 1) * 16 + gq * 4 + (j & 1) * 2;
;         nc.cm[j] = (((kc >= wstart) && (kc < wstart + 16)) ? 0xFFFFu : 0u) | (((kc + 1 >= wstart) && (kc + 1 < wstart + 16)) ? 0xFFFF0000u : 0u);
;     }
;     nc.blane = (unsigned)(size_t)(LAS unsigned char*)smem + 49152u + (unsigned)((16 + (cs + gq * 4 - qcol + 15)) * 4);
;     LAS unsigned char* ldsu = (LAS unsigned char*)smem;
;     const unsigned ldsa = (unsigned)(size_t)ldsu;
;     const int wuni = __builtin_amdgcn_readfirstlane(wid);
;     const bf16_t* kp0; const bf16_t* kp1; const bf16_t* vp0; const bf16_t* vp1;
;     {
;         const int ra = (wid * 2) * 8 + (lane >> 3), rb = (wid * 2 + 1) * 8 + (lane >> 3);
;         const int ca = ((lane & 7) ^ ((ra >> 1) & 7)) * 8, cb = ((lane & 7) ^ ((rb >> 1) & 7)) * 8;
;         kp0 = kbase + (size_t)ra * ldk + ca; kp1 = kbase + (size_t)rb * ldk + cb;
;         vp0 = vbase + (size_t)ra * TT + ca; vp1 = vbase + (size_t)rb * TT + cb;
;     }
;     ...
;     asm volatile("s_waitcnt lgkmcnt(0)" ::: "memory"); __builtin_amdgcn_s_barrier(); asm volatile("" ::: "memory");
;     ADMA(0);
;     if (ntile > 1) ADMA(1);
	s_nop 0
	v_lshl_add_u64 v[24:25], v[90:91], 0, v[22:23]
	v_lshl_add_u64 v[18:19], v[20:21], 0, v[18:19]
	global_load_lds_dwordx4 v[24:25], off
	v_lshl_add_u64 v[22:23], v[92:93], 0, v[22:23]
	s_mov_b32 m0, s0
	v_lshlrev_b64 v[18:19], 1, v[18:19]
	s_movk_i32 s6, 0xff00
	v_add_u32_e32 v21, 0x6000, v26
	global_load_lds_dwordx4 v[22:23], off
	v_lshl_add_u64 v[22:23], v[94:95], 0, v[18:19]
	s_mov_b32 s7, -1
	v_readfirstlane_b32 s0, v21
	v_lshl_add_u64 v[22:23], v[22:23], 0, s[6:7]
	s_mov_b32 m0, s0
	v_add_u32_e32 v21, 0x6400, v26
	global_load_lds_dwordx4 v[22:23], off
	v_lshl_add_u64 v[22:23], v[96:97], 0, v[18:19]
	v_readfirstlane_b32 s0, v21
	v_lshl_add_u64 v[22:23], v[22:23], 0, s[6:7]
	s_mov_b32 m0, s0
	v_add_u32_e32 v21, 0x2000, v26
	global_load_lds_dwordx4 v[22:23], off
	v_or_b32_e32 v22, 64, v86
	v_ashrrev_i32_e32 v23, 31, v22
	v_lshlrev_b64 v[22:23], 8, v[22:23]
	v_readfirstlane_b32 s0, v21
	v_add_u32_e32 v21, 0x2400, v26
	v_lshl_add_u64 v[24:25], v[90:91], 0, v[22:23]
	s_mov_b32 m0, s0
	v_readfirstlane_b32 s0, v21
	global_load_lds_dwordx4 v[24:25], off
	v_lshl_add_u64 v[22:23], v[92:93], 0, v[22:23]
	s_mov_b32 m0, s0
	v_or_b32_e32 v18, 0x80, v18
	v_add_u32_e32 v21, 0x8000, v26
	global_load_lds_dwordx4 v[22:23], off
	v_lshl_add_u64 v[22:23], v[94:95], 0, v[18:19]
	v_readfirstlane_b32 s0, v21
	v_add_u32_e32 v21, 0x8400, v26
	v_lshl_add_u64 v[22:23], v[22:23], 0, s[6:7]
	s_mov_b32 m0, s0
	v_lshl_add_u64 v[18:19], v[96:97], 0, v[18:19]
	v_readfirstlane_b32 s0, v21
	global_load_lds_dwordx4 v[22:23], off
	v_lshl_add_u64 v[18:19], v[18:19], 0, s[6:7]
	s_mov_b32 m0, s0
	v_cmp_gt_i32_e32 vcc, 63, v30
	global_load_lds_dwordx4 v[18:19], off
	s_nop 0
	v_cndmask_b32_e64 v18, 4, 6, vcc
	s_mov_b32 s0, 0x3fb8aa3b
	v_sub_u32_e32 v101, v18, v85
	s_waitcnt vmcnt(8)
	v_fma_f32 v18, v34, s0, -v100
	v_exp_f32_e32 v38, v18
	v_bfe_u32 v18, v31, 1, 3
	v_xor_b32_e32 v21, v32, v18
	v_lshlrev_b32_e32 v103, 4, v21
	v_bitop3_b32 v21, v32, v18, 4 bitop3:0x36
	v_lshlrev_b32_e32 v104, 4, v21
	v_bfe_u32 v21, v31, 5, 1
	s_movk_i32 s0, 0x110
	v_lshrrev_b32_e32 v19, 1, v31
	v_lshlrev_b32_e32 v88, 2, v32
	v_xor_b32_e32 v22, v21, v18
	v_bitop3_b32 v23, v21, v18, 2 bitop3:0x36
	v_bitop3_b32 v24, v21, v18, 4 bitop3:0x36
	v_bitop3_b32 v18, v21, v18, 6 bitop3:0x36
	v_or3_b32 v21, v33, v83, s0
	v_and_b32_e32 v19, 8, v19
	v_lshlrev_b32_e32 v22, 4, v22
	v_lshlrev_b32_e32 v23, 4, v23
	v_lshlrev_b32_e32 v24, 4, v24
	v_lshlrev_b32_e32 v18, 4, v18
	v_sub_u32_e32 v21, v21, v88
	s_movk_i32 s0, 0x6000
	v_mov_b32_e32 v62, v99
	v_mov_b32_e32 v63, v99
	v_mov_b32_e32 v64, v99
	v_mov_b32_e32 v65, v99
	v_and_b32_e32 v87, 63, v31
	v_sub_u32_e32 v110, v21, v20
	v_or3_b32 v111, v24, v19, s0
	v_or3_b32 v113, v22, v19, s0
	v_or3_b32 v125, v18, v19, s0
	v_or3_b32 v126, v23, v19, s0
	v_mov_b64_e32 v[58:59], v[62:63]
	v_mov_b64_e32 v[68:69], v[64:65]
	v_mov_b64_e32 v[30:31], v[62:63]
	v_mov_b64_e32 v[34:35], v[62:63]
	v_mov_b64_e32 v[18:19], v[62:63]
	v_mov_b64_e32 v[42:43], v[62:63]
	v_mov_b64_e32 v[22:23], v[62:63]
	v_mov_b64_e32 v[46:47], v[62:63]
	v_mov_b64_e32 v[50:51], v[62:63]
	v_mov_b64_e32 v[54:55], v[62:63]
	s_mov_b32 s72, 2
	s_mov_b32 s73, 0
	v_lshlrev_b32_e32 v98, 6, v82
	v_add_u32_e32 v102, 4, v101
	v_add_u32_e32 v105, 0xffffff9f, v84
	v_add_u32_e32 v106, 0x41, v84
	v_add_u32_e32 v107, 0x9f, v84
	v_add_u32_e32 v108, 0xffffff80, v84
	v_sub_u32_e32 v109, 0, v101
	v_lshl_add_u32 v112, v83, 7, v114
	s_mov_b64 s[82:83], 0
	v_mov_b64_e32 v[60:61], v[64:65]
	v_mov_b64_e32 v[66:67], v[62:63]
	v_mov_b64_e32 v[32:33], v[64:65]
	v_mov_b64_e32 v[36:37], v[64:65]
	v_mov_b64_e32 v[20:21], v[64:65]
	v_mov_b64_e32 v[44:45], v[64:65]
	v_mov_b64_e32 v[24:25], v[64:65]
	v_mov_b64_e32 v[48:49], v[64:65]
	v_mov_b64_e32 v[52:53], v[64:65]
	s_mov_b32 s8, 0
	v_mov_b64_e32 v[56:57], v[64:65]
	v_mov_b32_e32 v39, v38
	v_mov_b32_e32 v40, v38
	v_mov_b32_e32 v41, v38
	v_mov_b32_e32 v26, v38
	v_mov_b32_e32 v27, v38
	v_mov_b32_e32 v28, v38
	v_mov_b32_e32 v29, v38
	s_branch .LBB0_405
